# speedup vs baseline: 1.1125x; 1.0057x over previous
.Lret2:
	v_lshrrev_b32_e32 v151, 4, v120
	v_lshl_add_u32 v152, v123, 4, v131
	v_lshlrev_b32_e32 v153, 4, v123
	v_lshlrev_b32_e32 v154, 1, v121
	v_lshrrev_b32_e32 v155, 4, v122
	v_lshl_add_u32 v152, v151, 2, v152
	v_or_b32_e32 v155, v154, v155
	v_sub_u32_e32 v174, 11, v154
	v_lshl_or_b32 v156, v155, 8, v153
	v_cvt_f32_i32_e32 v174, v174
	v_cmp_lt_u32_e32 vcc, 31, v0
	v_add_u32_e32 v157, 0x4c00, v156
	v_mul_f32_e32 v175, 0xbf38aa3b, v174
	v_add_u32_e32 v158, 0xe400, v156
	v_mul_f32_e32 v175, v175, v174
	v_exp_f32_e32 v175, v175
	s_nop 0
	v_cndmask_b32_e32 v174, 1.0, v175, vcc
	s_waitcnt vmcnt(9)
	v_cvt_pk_f16_f32 v79, v8, v9
	v_cvt_pk_f16_f32 v78, v6, v7
	ds_write_b64 v141, v[78:79] offset:19456
	s_waitcnt vmcnt(8)
	v_cvt_pk_f16_f32 v79, v12, v13
	v_cvt_pk_f16_f32 v78, v10, v11
	ds_write_b64 v143, v[78:79] offset:19456
	s_waitcnt vmcnt(7)
	v_cvt_pk_f16_f32 v79, v20, v21
	v_cvt_pk_f16_f32 v78, v18, v19
	ds_write_b64 v144, v[78:79] offset:19456
	s_waitcnt vmcnt(6)
	v_cvt_pk_f16_f32 v79, v24, v25
	v_cvt_pk_f16_f32 v78, v22, v23
	ds_write_b64 v145, v[78:79] offset:19456
	s_waitcnt vmcnt(5)
	v_cvt_pk_f16_f32 v79, v28, v29
	v_cvt_pk_f16_f32 v78, v26, v27
	ds_write_b64 v146, v[78:79] offset:19456
	s_waitcnt vmcnt(4)
	v_cvt_pk_f16_f32 v79, v32, v33
	v_cvt_pk_f16_f32 v78, v30, v31
	ds_write_b64 v147, v[78:79] offset:19456
	s_waitcnt vmcnt(3)
	v_cvt_pk_f16_f32 v79, v40, v41
	v_cvt_pk_f16_f32 v78, v38, v39
	ds_write_b64 v141, v[78:79] offset:22568
	s_waitcnt vmcnt(2)
	v_cvt_pk_f16_f32 v79, v44, v45
	v_cvt_pk_f16_f32 v78, v42, v43
	ds_write_b64 v148, v[78:79] offset:19456
	s_waitcnt vmcnt(1)
	v_cvt_pk_f16_f32 v79, v52, v53
	v_cvt_pk_f16_f32 v78, v50, v51
	ds_write_b64 v149, v[78:79] offset:19456
	s_mov_b32 s3, 3
	v_mov_b32_e32 v86, 0
	v_mov_b32_e32 v78, 0
	v_mov_b32_e32 v79, 0
	v_mov_b32_e32 v80, 0
	v_mov_b32_e32 v81, 0
	v_mov_b32_e32 v82, 0
	v_mov_b32_e32 v83, 0
	v_mov_b32_e32 v84, 0
	v_mov_b32_e32 v85, 0
	ds_read_b128 v[194:197], v142
	ds_read_b128 v[198:201], v136
	ds_read_b128 v[202:205], v136 offset:9728
	ds_read_b128 v[206:209], v142 offset:64
	ds_read_b128 v[210:213], v136 offset:64
	ds_read_b128 v[214:217], v136 offset:9792
	ds_read_b128 v[218:221], v142 offset:128
	ds_read_b128 v[222:225], v136 offset:128
	ds_read_b128 v[226:229], v136 offset:9856
	ds_read_b128 v[230:233], v142 offset:192
	ds_read_b128 v[234:237], v136 offset:192
	ds_read_b128 v[238:241], v136 offset:9920
	s_waitcnt lgkmcnt(9)
	v_mfma_f32_16x16x32_f16 v[78:81], v[194:197], v[198:201], v[78:81]
	v_dot2c_f32_f16_e32 v86, v194, v194
	v_dot2c_f32_f16_e32 v86, v195, v195
	v_mfma_f32_16x16x32_f16 v[82:85], v[194:197], v[202:205], v[82:85]
	v_dot2c_f32_f16_e32 v86, v196, v196
	v_dot2c_f32_f16_e32 v86, v197, v197
	ds_read_b128 v[194:197], v142 offset:256
	ds_read_b128 v[198:201], v136 offset:256
	ds_read_b128 v[202:205], v136 offset:9984
	s_waitcnt lgkmcnt(9)
	v_mfma_f32_16x16x32_f16 v[78:81], v[206:209], v[210:213], v[78:81]
	v_dot2c_f32_f16_e32 v86, v206, v206
	v_dot2c_f32_f16_e32 v86, v207, v207
	v_mfma_f32_16x16x32_f16 v[82:85], v[206:209], v[214:217], v[82:85]
	v_dot2c_f32_f16_e32 v86, v208, v208
	v_dot2c_f32_f16_e32 v86, v209, v209
	ds_read_b128 v[206:209], v142 offset:320
	ds_read_b128 v[210:213], v136 offset:320
	ds_read_b128 v[214:217], v136 offset:10048
	s_waitcnt lgkmcnt(9)
	v_mfma_f32_16x16x32_f16 v[78:81], v[218:221], v[222:225], v[78:81]
	v_dot2c_f32_f16_e32 v86, v218, v218
	v_dot2c_f32_f16_e32 v86, v219, v219
	v_mfma_f32_16x16x32_f16 v[82:85], v[218:221], v[226:229], v[82:85]
	v_dot2c_f32_f16_e32 v86, v220, v220
	v_dot2c_f32_f16_e32 v86, v221, v221
	s_waitcnt lgkmcnt(6)
	v_mfma_f32_16x16x32_f16 v[78:81], v[230:233], v[234:237], v[78:81]
	v_dot2c_f32_f16_e32 v86, v230, v230
	v_dot2c_f32_f16_e32 v86, v231, v231
	v_mfma_f32_16x16x32_f16 v[82:85], v[230:233], v[238:241], v[82:85]
	v_dot2c_f32_f16_e32 v86, v232, v232
	v_dot2c_f32_f16_e32 v86, v233, v233
	s_waitcnt lgkmcnt(3)
	v_mfma_f32_16x16x32_f16 v[78:81], v[194:197], v[198:201], v[78:81]
	v_dot2c_f32_f16_e32 v86, v194, v194
	v_dot2c_f32_f16_e32 v86, v195, v195
	v_mfma_f32_16x16x32_f16 v[82:85], v[194:197], v[202:205], v[82:85]
	v_dot2c_f32_f16_e32 v86, v196, v196
	v_dot2c_f32_f16_e32 v86, v197, v197
	s_waitcnt lgkmcnt(0)
	v_mfma_f32_16x16x32_f16 v[78:81], v[206:209], v[210:213], v[78:81]
	v_dot2c_f32_f16_e32 v86, v206, v206
	v_dot2c_f32_f16_e32 v86, v207, v207
	v_mfma_f32_16x16x32_f16 v[82:85], v[206:209], v[214:217], v[82:85]
	v_dot2c_f32_f16_e32 v86, v208, v208
	v_dot2c_f32_f16_e32 v86, v209, v209
	ds_read_b128 v[222:225], v136 offset:384
	ds_read_b128 v[226:229], v136 offset:10112
	ds_read_b128 v[234:237], v136 offset:448
	ds_read_b128 v[238:241], v136 offset:10176
	ds_read_b128 v[198:201], v136 offset:512
	ds_read_b128 v[202:205], v136 offset:10240
	ds_read2st64_b64 v[88:91], v160 offset0:1 offset1:20
	s_waitcnt vmcnt(0)
	v_cvt_pk_f16_f32 v163, v188, v189
	v_cvt_pk_f16_f32 v162, v186, v187
	s_and_saveexec_b64 s[12:13], s[8:9]
	ds_write_b64 v150, v[162:163] offset:19456
	s_or_b64 exec, exec, s[12:13]
	ds_read_b128 v[218:221], v142 offset:384
	ds_read_b128 v[230:233], v142 offset:448
	ds_read_b128 v[194:197], v142 offset:512
	ds_read_b64 v[92:93], v159 offset:20032
	s_waitcnt lgkmcnt(3)
	v_mfma_f32_16x16x32_f16 v[78:81], v[218:221], v[222:225], v[78:81]
	v_dot2c_f32_f16_e32 v86, v218, v218
	v_dot2c_f32_f16_e32 v86, v219, v219
	v_mfma_f32_16x16x32_f16 v[82:85], v[218:221], v[226:229], v[82:85]
	v_dot2c_f32_f16_e32 v86, v220, v220
	v_dot2c_f32_f16_e32 v86, v221, v221
	s_waitcnt lgkmcnt(2)
	v_mfma_f32_16x16x32_f16 v[78:81], v[230:233], v[234:237], v[78:81]
	v_dot2c_f32_f16_e32 v86, v230, v230
	v_dot2c_f32_f16_e32 v86, v231, v231
	v_mfma_f32_16x16x32_f16 v[82:85], v[230:233], v[238:241], v[82:85]
	v_dot2c_f32_f16_e32 v86, v232, v232
	v_dot2c_f32_f16_e32 v86, v233, v233
	s_waitcnt lgkmcnt(1)
	v_mfma_f32_16x16x32_f16 v[78:81], v[194:197], v[198:201], v[78:81]
	v_dot2c_f32_f16_e32 v86, v194, v194
	v_dot2c_f32_f16_e32 v86, v195, v195
	v_mfma_f32_16x16x32_f16 v[82:85], v[194:197], v[202:205], v[82:85]
	v_dot2c_f32_f16_e32 v86, v196, v196
	v_dot2c_f32_f16_e32 v86, v197, v197
	s_waitcnt lgkmcnt(0)
	v_mfma_f32_16x16x16_f16 v[78:81], v[92:93], v[88:89], v[78:81]
	v_dot2c_f32_f16_e32 v86, v92, v92
	v_dot2c_f32_f16_e32 v86, v93, v93
	v_mfma_f32_16x16x16_f16 v[82:85], v[92:93], v[90:91], v[82:85]
	s_branch .Lnorm

.LBB0_20:
	ds_write2st64_b32 v152, v94, v95 offset0:76 offset1:77
	ds_write2st64_b32 v152, v98, v99 offset0:78 offset1:79
	ds_write2st64_b32 v152, v100, v101 offset0:80 offset1:81
	ds_write2st64_b32 v152, v102, v103 offset0:82 offset1:83
	ds_write2st64_b32 v152, v104, v105 offset0:84 offset1:85
	ds_write2st64_b32 v152, v106, v107 offset0:86 offset1:87
	ds_write2st64_b32 v152, v108, v109 offset0:88 offset1:89
	ds_write2st64_b32 v152, v110, v111 offset0:90 offset1:91
	ds_write2st64_b32 v152, v112, v113 offset0:92 offset1:93
	ds_write2st64_b32 v152, v114, v115 offset0:94 offset1:95
	ds_write2st64_b32 v152, v116, v117 offset0:96 offset1:97
	v_mov_b32_e32 v3, 0
	s_waitcnt lgkmcnt(0)
	s_barrier
	s_and_saveexec_b64 s[4:5], s[0:1]
	s_cbranch_execz .LBB0_22
	ds_read_b128 v[10:13], v157
	ds_read_b128 v[14:17], v157 offset:9728
	ds_read_b128 v[18:21], v157 offset:19456
	ds_read_b128 v[22:25], v157 offset:29184
	ds_read_b128 v[26:29], v158
	ds_read_b128 v[30:33], v158 offset:9728
	ds_read_b128 v[34:37], v158 offset:19456
	ds_read_b128 v[38:41], v158 offset:29184
	s_waitcnt lgkmcnt(4)
	v_add_f32_e32 v10, v10, v11
	v_add_f32_e32 v12, v12, v13
	v_add_f32_e32 v14, v14, v15
	v_add_f32_e32 v16, v16, v17
	v_add_f32_e32 v18, v18, v19
	v_add_f32_e32 v20, v20, v21
	v_add_f32_e32 v22, v22, v23
	v_add_f32_e32 v24, v24, v25
	v_add_f32_e32 v10, v10, v12
	v_add_f32_e32 v14, v14, v16
	v_add_f32_e32 v18, v18, v20
	v_add_f32_e32 v22, v22, v24
	v_add_f32_e32 v10, v10, v14
	v_add_f32_e32 v18, v18, v22
	v_add_f32_e32 v10, v10, v18
	s_waitcnt lgkmcnt(0)
	v_add_f32_e32 v26, v26, v27
	v_add_f32_e32 v28, v28, v29
	v_add_f32_e32 v30, v30, v31
	v_add_f32_e32 v32, v32, v33
	v_add_f32_e32 v34, v34, v35
	v_add_f32_e32 v36, v36, v37
	v_add_f32_e32 v38, v38, v39
	v_add_f32_e32 v40, v40, v41
	v_add_f32_e32 v26, v26, v28
	v_add_f32_e32 v30, v30, v32
	v_add_f32_e32 v34, v34, v36
	v_add_f32_e32 v38, v38, v40
	v_add_f32_e32 v26, v26, v30
	v_add_f32_e32 v34, v34, v38
	v_add_f32_e32 v26, v26, v34
	v_add_f32_e32 v2, v10, v26
	v_mul_f32_e32 v2, v174, v2
	v_max_f32_e32 v2, 0x2edbe6ff, v2
	v_log_f32_e32 v2, v2
	v_cmp_lt_i32_e32 vcc, 1, v119
	v_mul_f32_e32 v2, v118, v2
	s_nop 0
	v_cndmask_b32_e32 v3, 0, v2, vcc
